# MoE M3 unit switch: next unit's flag polled before the stage's DMA loads (vmcnt(6) instead of a full drain); blocking poll loop kept as fallback
# speedup vs baseline: 1.0302x; 1.0012x over previous
.LBB0_1265:
	s_mul_i32 s4, s24, 0xc000
	s_add_i32 s4, s4, 0
	v_add3_u32 v128, s4, v204, v205
	s_barrier
	v_add_u32_e32 v129, 0x4000, v128
	ds_read2_b64 v[136:139], v129 offset1:16
	ds_read2_b64 v[144:147], v129 offset0:128 offset1:144
	v_add_u32_e32 v129, 0x4800, v128
	ds_read2_b64 v[152:155], v129 offset1:16
	ds_read2_b64 v[160:163], v129 offset0:128 offset1:144
	v_add_u32_e32 v129, 0x5000, v128
	v_add_u32_e32 v128, 0x5800, v128
	s_add_i32 s4, s4, s11
	ds_read2_b64 v[168:171], v129 offset1:16
	ds_read2_b64 v[176:179], v129 offset0:128 offset1:144
	ds_read2_b64 v[184:187], v128 offset1:16
	ds_read2_b64 v[188:191], v128 offset0:128 offset1:144
	v_add_u32_e32 v128, s4, v203
	ds_read_b128 v[180:183], v128
	ds_read_b128 v[172:175], v128 offset:1024
	ds_read_b128 v[164:167], v128 offset:2048
	ds_read_b128 v[156:159], v128 offset:3072
	ds_read_b128 v[148:151], v128 offset:4096
	ds_read_b128 v[140:143], v128 offset:5120
	ds_read_b128 v[132:135], v128 offset:6144
	ds_read_b128 v[128:131], v128 offset:7168
	s_cmp_ge_i32 s18, s10
	s_cbranch_scc1 .LBB0_1260
	s_cmp_lg_u32 s6, 15
	s_cbranch_scc1 .Lm3pp_skip
	s_add_i32 s100, s15, 1
	s_cmp_ge_i32 s100, s12
	s_cbranch_scc1 .Lm3pp_skip
	s_mul_i32 s100, s100, 12
	s_add_i32 s100, s100, 0x24190
	v_mov_b32_e32 v214, s100
	ds_read2_b32 v[214:215], v214 offset1:1
	v_mov_b32_e32 v248, 0
	s_waitcnt lgkmcnt(0)
	v_readfirstlane_b32 s100, v214
	v_readfirstlane_b32 s101, v215
	s_lshl_b32 s100, s100, 9
	s_lshl_b32 s101, s101, 4
	s_add_i32 s100, s101, s100
	s_ashr_i32 s101, s100, 31
	s_lshl_b64 s[100:101], s[100:101], 2
	s_add_u32 s100, s20, s100
	s_addc_u32 s101, s21, s101
	global_load_dword v248, v209, s[100:101] sc1
.Lm3pp_skip:
	s_mul_i32 s4, s19, 0xc000
	s_lshl_b32 s5, s6, 6
	s_add_i32 s7, s13, s4
	v_add_u32_e32 v195, s5, v220
	s_mov_b32 m0, s7
	s_lshl_b32 s4, s6, 5
	global_load_lds_dwordx4 v195, s[2:3]
	v_add_u32_e32 v195, s5, v221
	s_ashr_i32 s5, s4, 31
	s_lshl_b64 s[8:9], s[4:5], 13
	v_lshl_add_u64 v[212:213], v[196:197], 0, s[8:9]
	s_or_b32 s8, s4, 8
	s_add_i32 m0, s7, 0x2000
	s_ashr_i32 s9, s8, 31
	global_load_lds_dwordx4 v195, s[2:3]
	s_add_i32 m0, s7, 0x4000
	s_lshl_b64 s[8:9], s[8:9], 13
	global_load_lds_dwordx4 v[212:213], off
	v_lshl_add_u64 v[212:213], v[198:199], 0, s[8:9]
	s_or_b32 s8, s4, 16
	s_ashr_i32 s9, s8, 31
	s_or_b32 s4, s4, 24
	s_add_i32 m0, s7, 0x6000
	s_lshl_b64 s[8:9], s[8:9], 13
	s_ashr_i32 s5, s4, 31
	global_load_lds_dwordx4 v[212:213], off
	v_lshl_add_u64 v[212:213], v[196:197], 0, s[8:9]
	s_add_i32 m0, s7, 0x8000
	s_lshl_b64 s[4:5], s[4:5], 13
	global_load_lds_dwordx4 v[212:213], off
	v_lshl_add_u64 v[212:213], v[198:199], 0, s[4:5]
	s_add_i32 m0, s7, 0xa000
	s_add_i32 s4, s19, 1
	global_load_lds_dwordx4 v[212:213], off
	s_cmp_lg_u32 s19, 2
	s_cselect_b32 s19, s4, 0
	s_add_i32 s6, s6, 1
	s_cmp_lg_u32 s6, 16
	s_cbranch_scc1 .LBB0_1259
	s_add_i32 s15, s15, 1
	s_cmp_ge_i32 s15, s12
	s_cbranch_scc1 .LBB0_1258
	s_mul_i32 s4, s15, 12
	s_add_i32 s4, s4, 0
	s_add_i32 s4, s4, 0x24190
	v_mov_b32_e32 v195, s4
	ds_read2_b32 v[196:197], v195 offset1:1
	ds_read_b32 v195, v195 offset:8
	s_waitcnt lgkmcnt(0)
	v_readfirstlane_b32 s4, v196
	v_readfirstlane_b32 s5, v197
	s_lshl_b32 s6, s4, 9
	s_lshl_b32 s5, s5, 4
	s_add_i32 s6, s5, s6
	s_ashr_i32 s7, s6, 31
	s_lshl_b64 s[6:7], s[6:7], 2
	s_add_u32 s6, s20, s6
	s_addc_u32 s7, s21, s7
	s_waitcnt vmcnt(6)
	v_cmp_lt_u32_e32 vcc, 3, v248
	s_cbranch_vccnz .LBB0_1257
	s_mov_b32 s5, 0x400001
	s_branch .LBB0_1270

	.amdhsa_kernel _Z6mk_fwd4Args
		.amdhsa_group_segment_fixed_size 0
		.amdhsa_private_segment_fixed_size 0
		.amdhsa_kernarg_size 584
		.amdhsa_user_sgpr_count 2
		.amdhsa_user_sgpr_dispatch_ptr 0
		.amdhsa_user_sgpr_queue_ptr 0
		.amdhsa_user_sgpr_kernarg_segment_ptr 1
		.amdhsa_user_sgpr_dispatch_id 0
		.amdhsa_user_sgpr_kernarg_preload_length 0
		.amdhsa_user_sgpr_kernarg_preload_offset 0
		.amdhsa_user_sgpr_private_segment_size 0
		.amdhsa_uses_dynamic_stack 0
		.amdhsa_enable_private_segment 0
		.amdhsa_system_sgpr_workgroup_id_x 1
		.amdhsa_system_sgpr_workgroup_id_y 0
		.amdhsa_system_sgpr_workgroup_id_z 0
		.amdhsa_system_sgpr_workgroup_info 0
		.amdhsa_system_vgpr_workitem_id 0
		.amdhsa_next_free_vgpr 256
		.amdhsa_next_free_sgpr 102
		.amdhsa_accum_offset 256
		.amdhsa_reserve_vcc 1
		.amdhsa_float_round_mode_32 0
		.amdhsa_float_round_mode_16_64 0
		.amdhsa_float_denorm_mode_32 3
		.amdhsa_float_denorm_mode_16_64 3
		.amdhsa_dx10_clamp 1
		.amdhsa_ieee_mode 1
		.amdhsa_fp16_overflow 0
		.amdhsa_tg_split 0
		.amdhsa_exception_fp_ieee_invalid_op 0
		.amdhsa_exception_fp_denorm_src 0
		.amdhsa_exception_fp_ieee_div_zero 0
		.amdhsa_exception_fp_ieee_overflow 0
		.amdhsa_exception_fp_ieee_underflow 0
		.amdhsa_exception_fp_ieee_inexact 0
		.amdhsa_exception_int_div_zero 0
	.end_amdhsa_kernel

amdhsa.kernels:
  - .agpr_count:     0
    .args:
      - .offset:         0
        .size:           328
        .value_kind:     by_value
      - .offset:         328
        .size:           4
        .value_kind:     hidden_block_count_x
      - .offset:         332
        .size:           4
        .value_kind:     hidden_block_count_y
      - .offset:         336
        .size:           4
        .value_kind:     hidden_block_count_z
      - .offset:         340
        .size:           2
        .value_kind:     hidden_group_size_x
      - .offset:         342
        .size:           2
        .value_kind:     hidden_group_size_y
      - .offset:         344
        .size:           2
        .value_kind:     hidden_group_size_z
      - .offset:         346
        .size:           2
        .value_kind:     hidden_remainder_x
      - .offset:         348
        .size:           2
        .value_kind:     hidden_remainder_y
      - .offset:         350
        .size:           2
        .value_kind:     hidden_remainder_z
      - .offset:         368
        .size:           8
        .value_kind:     hidden_global_offset_x
      - .offset:         376
        .size:           8
        .value_kind:     hidden_global_offset_y
      - .offset:         384
        .size:           8
        .value_kind:     hidden_global_offset_z
      - .offset:         392
        .size:           2
        .value_kind:     hidden_grid_dims
      - .offset:         448
        .size:           4
        .value_kind:     hidden_dynamic_lds_size
    .group_segment_fixed_size: 0
    .kernarg_segment_align: 8
    .kernarg_segment_size: 584
    .language:       OpenCL C
    .language_version:
      - 2
      - 0
    .max_flat_workgroup_size: 512
    .name:           _Z6mk_fwd4Args
    .private_segment_fixed_size: 0
    .sgpr_count:     108
    .sgpr_spill_count: 95
    .symbol:         _Z6mk_fwd4Args.kd
    .uniform_work_group_size: 1
    .uses_dynamic_stack: false
    .vgpr_count:     256
    .vgpr_spill_count: 0
    .wavefront_size: 64
